# GLA state update: 8 packed v_pk_mul_f32 between the MFMAs split into scalar v_mul_f32 pairs (bit-identical; packed f32 ops feeding MFMA operands issue slower)
# baseline (speedup 1.0000x reference)
.Lgo_pos:
	v_lshl_add_u32 v251, v215, 9, v218
	v_add_u32_e32 v252, s0, v251
	v_add_u32_e32 v253, s1, v251
	v_add_u32_e32 v216, s1, v252
	ds_read_b128 v[30:33], v97 offset:9216
	ds_read_b128 v[40:43], v97 offset:9280
	ds_read_b128 v[44:47], v97 offset:11520
	ds_read_b128 v[52:55], v97 offset:2304
	ds_read_b128 v[60:63], v97 offset:11584
	ds_read_b128 v[64:67], v97 offset:2368
	ds_read_b128 v[72:75], v98 offset:9216
	ds_read_b128 v[142:145], v98
	ds_read_b128 v[146:149], v98 offset:9280
	ds_read_b128 v[150:153], v98 offset:64
	ds_read_b128 v[154:157], v99 offset:9216
	ds_read_b128 v[158:161], v99
	ds_read_b128 v[162:165], v99 offset:9280
	ds_read_b128 v[166:169], v99 offset:64
	ds_read_b128 v[48:51], v97 offset:64
	ds_read_b128 v[56:59], v97
	s_waitcnt lgkmcnt(0)
	v_mfma_f32_16x16x32_bf16 v[56:59], v[30:33], v[56:59], 0
	v_mfma_f32_16x16x32_bf16 v[48:51], v[40:43], v[48:51], v[56:59]
	s_nop 7
	v_cndmask_b32_e64 v35, v51, 0, s[40:41]
	v_cndmask_b32_e64 v141, v50, 0, s[62:63]
	v_cndmask_b32_e64 v170, v49, 0, s[72:73]
	v_cndmask_b32_e64 v171, v48, 0, s[2:3]
	v_mfma_f32_16x16x32_bf16 v[48:51], v[30:33], v[52:55], 0
	v_mfma_f32_16x16x32_bf16 v[56:59], v[40:43], v[64:67], v[48:51]
	v_mfma_f32_16x16x32_bf16 v[48:51], v[30:33], v[142:145], 0
	v_mfma_f32_16x16x32_bf16 v[30:33], v[30:33], v[158:161], 0
	v_mfma_f32_16x16x32_bf16 v[48:51], v[40:43], v[150:153], v[48:51]
	v_mfma_f32_16x16x32_bf16 v[40:43], v[40:43], v[166:169], v[30:33]
	v_mfma_f32_16x16x32_bf16 v[30:33], v[44:47], v[52:55], 0
	v_mfma_f32_16x16x32_bf16 v[30:33], v[60:63], v[64:67], v[30:33]
	v_cvt_pk_bf16_f32 v64, v26, v27
	v_cvt_pk_bf16_f32 v65, v28, v29
	v_cvt_pk_bf16_f32 v66, v36, v37
	v_cvt_pk_bf16_f32 v67, v38, v39
	s_nop 3
	v_cndmask_b32_e64 v172, v33, 0, s[40:41]
	v_cndmask_b32_e64 v173, v32, 0, s[62:63]
	v_cndmask_b32_e64 v174, v31, 0, s[72:73]
	v_cndmask_b32_e64 v175, v30, 0, s[2:3]
	v_mfma_f32_16x16x32_bf16 v[30:33], v[44:47], v[142:145], 0
	v_mfma_f32_16x16x32_bf16 v[68:71], v[60:63], v[150:153], v[30:33]
	v_mfma_f32_16x16x32_bf16 v[30:33], v[44:47], v[158:161], 0
	v_mfma_f32_16x16x32_bf16 v[52:55], v[60:63], v[166:169], v[30:33]
	v_cvt_pk_bf16_f32 v60, v18, v19
	v_cvt_pk_bf16_f32 v61, v20, v21
	v_cvt_pk_bf16_f32 v62, v22, v23
	v_mfma_f32_16x16x32_bf16 v[30:33], v[72:75], v[142:145], 0
	v_cvt_pk_bf16_f32 v63, v24, v25
	v_mfma_f32_16x16x32_bf16 v[30:33], v[146:149], v[150:153], v[30:33]
	s_nop 7
	v_cndmask_b32_e64 v150, v33, 0, s[40:41]
	v_cndmask_b32_e64 v151, v32, 0, s[62:63]
	v_cndmask_b32_e64 v152, v31, 0, s[72:73]
	v_cndmask_b32_e64 v153, v30, 0, s[2:3]
	v_mfma_f32_16x16x32_bf16 v[30:33], v[72:75], v[158:161], 0
	v_mfma_f32_16x16x32_bf16 v[44:47], v[146:149], v[166:169], v[30:33]
	v_mfma_f32_16x16x32_bf16 v[30:33], v[154:157], v[158:161], 0
	v_mfma_f32_16x16x32_bf16 v[30:33], v[162:165], v[166:169], v[30:33]
	s_nop 7
	v_cndmask_b32_e64 v157, v30, 0, s[2:3]
	v_add_u32_e32 v30, 0x6800, v106
	ds_read2_b64 v[142:145], v30 offset0:128 offset1:132
	ds_read2_b64 v[72:75], v30 offset0:136 offset1:140
	v_cndmask_b32_e64 v154, v33, 0, s[40:41]
	v_cndmask_b32_e64 v155, v32, 0, s[62:63]
	v_cvt_pk_bf16_f32 v32, v171, v170
	v_cvt_pk_bf16_f32 v33, v141, v35
	v_mov_b32_e32 v35, v34
	ds_read2_b64 v[146:149], v101 offset1:4
	v_cndmask_b32_e64 v156, v31, 0, s[72:73]
	s_waitcnt lgkmcnt(2)
	v_mfma_f32_16x16x32_bf16 v[30:33], v[142:145], v[32:35], 0
	s_waitcnt lgkmcnt(0)
	v_mfma_f32_16x16x32_bf16 v[30:33], v[60:63], v[146:149], v[30:33]
	ds_read2_b64 v[146:149], v101 offset0:8 offset1:12
	s_waitcnt lgkmcnt(0)
	v_mfma_f32_16x16x32_bf16 v[30:33], v[64:67], v[146:149], v[30:33]
	s_nop 7
	v_med3_f32 v30, v30, s75, v238
	v_med3_f32 v31, v31, s75, v238
	v_med3_f32 v32, v32, s75, v238
	v_med3_f32 v33, v33, s75, v238
	v_cvt_pk_fp8_f32 v247, v30, v31
	s_nop 1
	v_cvt_pk_fp8_f32 v247, v32, v33 op_sel:[0,0,1]
	s_nop 1
	global_store_dword v251, v247, s[94:95]
	v_cvt_pk_bf16_f32 v30, v56, v57
	v_cvt_pk_bf16_f32 v31, v58, v59
	v_cvt_pk_bf16_f32 v32, v175, v174
	v_cvt_pk_bf16_f32 v33, v173, v172
	ds_read2_b64 v[56:59], v102 offset1:4
	s_nop 0
	v_mfma_f32_16x16x32_bf16 v[30:33], v[142:145], v[30:33], 0
	s_waitcnt lgkmcnt(0)
	v_mfma_f32_16x16x32_bf16 v[30:33], v[60:63], v[56:59], v[30:33]
	ds_read2_b64 v[56:59], v102 offset0:8 offset1:12
	s_waitcnt lgkmcnt(0)
	v_mfma_f32_16x16x32_bf16 v[30:33], v[64:67], v[56:59], v[30:33]
	s_nop 7
	v_med3_f32 v30, v30, s75, v238
	v_med3_f32 v31, v31, s75, v238
	v_med3_f32 v32, v32, s75, v238
	v_med3_f32 v33, v33, s75, v238
	v_cvt_pk_fp8_f32 v248, v30, v31
	s_nop 1
	v_cvt_pk_fp8_f32 v248, v32, v33 op_sel:[0,0,1]
	s_nop 1
	global_store_dword v252, v248, s[94:95]
	v_cvt_pk_bf16_f32 v30, v48, v49
	v_cvt_pk_bf16_f32 v31, v50, v51
	v_cvt_pk_bf16_f32 v32, v68, v69
	v_cvt_pk_bf16_f32 v33, v70, v71
	s_nop 1
	v_mfma_f32_16x16x32_bf16 v[48:51], v[142:145], v[30:33], 0
	v_cvt_pk_bf16_f32 v32, v153, v152
	v_cvt_pk_bf16_f32 v33, v151, v150
	s_nop 1
	v_mfma_f32_16x16x32_bf16 v[30:33], v[72:75], v[32:35], v[48:51]
	v_add_u32_e32 v35, v95, v105
	s_nop 1
	ds_read2_b64 v[48:51], v103 offset1:4
	s_waitcnt lgkmcnt(0)
	v_mfma_f32_16x16x32_bf16 v[30:33], v[60:63], v[48:51], v[30:33]
	ds_read2_b64 v[48:51], v103 offset0:8 offset1:12
	s_waitcnt lgkmcnt(0)
	v_mfma_f32_16x16x32_bf16 v[30:33], v[64:67], v[48:51], v[30:33]
	s_nop 7
	v_med3_f32 v30, v30, s75, v238
	v_med3_f32 v31, v31, s75, v238
	v_med3_f32 v32, v32, s75, v238
	v_med3_f32 v33, v33, s75, v238
	v_cvt_pk_fp8_f32 v249, v30, v31
	s_nop 1
	v_cvt_pk_fp8_f32 v249, v32, v33 op_sel:[0,0,1]
	s_nop 1
	global_store_dword v253, v249, s[94:95]
	v_cvt_pk_bf16_f32 v30, v40, v41
	v_cvt_pk_bf16_f32 v31, v42, v43
	v_cvt_pk_bf16_f32 v32, v52, v53
	v_cvt_pk_bf16_f32 v33, v54, v55
	v_cvt_pk_bf16_f32 v40, v44, v45
	v_cvt_pk_bf16_f32 v41, v46, v47
	v_mfma_f32_16x16x32_bf16 v[30:33], v[142:145], v[30:33], 0
	v_cvt_pk_bf16_f32 v42, v157, v156
	v_cvt_pk_bf16_f32 v43, v155, v154
	v_add_u32_e32 v44, v95, v100
	s_nop 0
	v_mfma_f32_16x16x32_bf16 v[30:33], v[72:75], v[40:43], v[30:33]
	ds_read2_b64 v[40:43], v104 offset1:4
	s_waitcnt lgkmcnt(0)
	v_mfma_f32_16x16x32_bf16 v[30:33], v[60:63], v[40:43], v[30:33]
	ds_read2_b64 v[40:43], v104 offset0:8 offset1:12
	s_waitcnt lgkmcnt(0)
	v_mfma_f32_16x16x32_bf16 v[30:33], v[64:67], v[40:43], v[30:33]
	s_nop 7
	v_med3_f32 v30, v30, s75, v238
	v_med3_f32 v31, v31, s75, v238
	v_med3_f32 v32, v32, s75, v238
	v_med3_f32 v33, v33, s75, v238
	v_cvt_pk_fp8_f32 v250, v30, v31
	s_nop 1
	v_cvt_pk_fp8_f32 v250, v32, v33 op_sel:[0,0,1]
	s_nop 1
	global_store_dword v216, v250, s[94:95]
	ds_read_b128 v[30:33], v114 offset:48128
	ds_read_b128 v[40:43], v44 offset:18432
	s_waitcnt lgkmcnt(1)
	v_mul_f32_e32 v18, v18, v30
	v_mul_f32_e32 v19, v19, v31
	v_mul_f32_e32 v20, v20, v32
	v_mul_f32_e32 v21, v21, v33
	ds_read_b128 v[30:33], v114 offset:48192
	s_waitcnt lgkmcnt(0)
	v_mul_f32_e32 v22, v22, v30
	v_mul_f32_e32 v23, v23, v31
	v_mul_f32_e32 v24, v24, v32
	v_mul_f32_e32 v25, v25, v33
	ds_read_b128 v[30:33], v114 offset:48256
	s_waitcnt lgkmcnt(0)
	v_mul_f32_e32 v26, v26, v30
	v_mul_f32_e32 v27, v27, v31
	v_mul_f32_e32 v28, v28, v32
	v_mul_f32_e32 v29, v29, v33
	ds_read_b128 v[30:33], v114 offset:48320
	s_waitcnt lgkmcnt(0)
	v_mul_f32_e32 v30, v36, v30
	v_mul_f32_e32 v31, v37, v31
	v_mul_f32_e32 v32, v38, v32
	v_mul_f32_e32 v33, v39, v33
	ds_read_b128 v[36:39], v35 offset:27648
	s_waitcnt vmcnt(38)
	v_mov_b32_e32 v115, v178
	v_mov_b32_e32 v116, v179
	v_mov_b32_e32 v117, v180
	v_mov_b32_e32 v118, v181
	v_mov_b32_e32 v119, v182
	v_mov_b32_e32 v120, v183
	s_waitcnt lgkmcnt(0)
	v_mfma_f32_16x16x32_bf16 v[18:21], v[40:43], v[36:39], v[18:21]
	ds_read_b128 v[40:43], v44 offset:20736
	s_waitcnt vmcnt(32)
	v_mov_b32_e32 v121, v184
	v_mov_b32_e32 v122, v185
	v_mov_b32_e32 v123, v186
	v_mov_b32_e32 v124, v187
	v_mov_b32_e32 v125, v188
	v_mov_b32_e32 v128, v189
	s_waitcnt lgkmcnt(0)
	v_mfma_f32_16x16x32_bf16 v[22:25], v[40:43], v[36:39], v[22:25]
	ds_read_b128 v[40:43], v44 offset:23040
	s_waitcnt vmcnt(26)
	v_mov_b32_e32 v129, v190
	v_mov_b32_e32 v130, v192
	v_mov_b32_e32 v131, v194
	v_mov_b32_e32 v132, v196
	v_mov_b32_e32 v133, v200
	v_mov_b32_e32 v134, v201
	s_waitcnt lgkmcnt(0)
	v_mfma_f32_16x16x32_bf16 v[26:29], v[40:43], v[36:39], v[26:29]
	ds_read_b128 v[40:43], v44 offset:25344
	s_waitcnt vmcnt(20)
	v_mov_b32_e32 v135, v202
	v_mov_b32_e32 v136, v203
	v_mov_b32_e32 v137, v206
	v_mov_b32_e32 v138, v207
	v_mov_b32_e32 v139, v208
	v_mov_b32_e32 v140, v209
	s_waitcnt lgkmcnt(0)
	v_mfma_f32_16x16x32_bf16 v[30:33], v[40:43], v[36:39], v[30:33]
	ds_read_b128 v[36:39], v35 offset:27712
	ds_read_b128 v[40:43], v44 offset:18496
	s_waitcnt vmcnt(16)
	v_mov_b32_e32 v2, v220
	v_mov_b32_e32 v1, v219
	v_mov_b32_e32 v4, v222
	v_mov_b32_e32 v3, v221
	s_waitcnt lgkmcnt(0)
	v_mfma_f32_16x16x32_bf16 v[18:21], v[40:43], v[36:39], v[18:21]
	ds_read_b128 v[40:43], v44 offset:20800
	s_waitcnt vmcnt(12)
	v_mov_b32_e32 v6, v224
	v_mov_b32_e32 v5, v223
	v_mov_b32_e32 v8, v226
	v_mov_b32_e32 v7, v225
	s_waitcnt lgkmcnt(0)
	v_mfma_f32_16x16x32_bf16 v[22:25], v[40:43], v[36:39], v[22:25]
	ds_read_b128 v[40:43], v44 offset:23104
	s_waitcnt vmcnt(8)
	v_mov_b32_e32 v10, v228
	v_mov_b32_e32 v9, v227
	v_mov_b32_e32 v12, v230
	v_mov_b32_e32 v11, v229
	s_waitcnt lgkmcnt(0)
	v_mfma_f32_16x16x32_bf16 v[26:29], v[40:43], v[36:39], v[26:29]
	ds_read_b128 v[40:43], v44 offset:25408
	s_waitcnt vmcnt(4)
	v_mov_b32_e32 v14, v232
	v_mov_b32_e32 v13, v231
	v_mov_b32_e32 v16, v246
	v_mov_b32_e32 v15, v233
	s_waitcnt lgkmcnt(0)
	v_mfma_f32_16x16x32_bf16 v[36:39], v[40:43], v[36:39], v[30:33]
	s_nop 2
	s_branch .LBB0_468
